# baseline (speedup 1.0000x reference)
.LBB1_21:
	ds_read_b128 v[48:51], v46 offset:32768
	ds_read_b128 v[52:55], v46 offset:33792
	ds_read_b128 v[56:59], v46 offset:34816
	ds_read_b128 v[60:63], v46 offset:35840
	s_add_i32 s60, s55, 2
	s_cmp_eq_u32 s49, s55
	s_cselect_b32 s57, s21, s25
	s_cselect_b32 s56, s20, s24
	s_cselect_b32 s59, s5, s23
	s_cselect_b32 s58, s4, s22
	ds_read_b128 v[64:67], v47
	ds_read_b128 v[68:71], v47 offset:1024
	ds_read_b128 v[72:75], v47 offset:2048
	ds_read_b128 v[76:79], v47 offset:3072
	ds_read_b128 v[80:83], v47 offset:4096
	ds_read_b128 v[84:87], v47 offset:5120
	ds_read_b128 v[88:91], v47 offset:6144
	ds_read_b128 v[92:95], v47 offset:7168
	s_waitcnt lgkmcnt(0)
	s_barrier
	s_waitcnt lgkmcnt(0)
	s_setprio 1
	s_waitcnt lgkmcnt(0)
	v_mfma_f32_16x16x32_f16 v[28:31], v[48:51], v[64:67], v[28:31]
	v_mfma_f32_16x16x32_f16 v[24:27], v[56:59], v[64:67], v[24:27]
	v_mfma_f32_16x16x32_f16 v[20:23], v[48:51], v[72:75], v[20:23]
	v_mfma_f32_16x16x32_f16 v[16:19], v[56:59], v[72:75], v[16:19]
	v_mfma_f32_16x16x32_f16 v[12:15], v[48:51], v[80:83], v[12:15]
	v_mfma_f32_16x16x32_f16 v[8:11], v[56:59], v[80:83], v[8:11]
	v_mfma_f32_16x16x32_f16 v[4:7], v[48:51], v[88:91], v[4:7]
	v_mfma_f32_16x16x32_f16 v[0:3], v[56:59], v[88:91], v[0:3]
	v_mfma_f32_16x16x32_f16 v[28:31], v[52:55], v[68:71], v[28:31]
	v_mfma_f32_16x16x32_f16 v[24:27], v[60:63], v[68:71], v[24:27]
	v_mfma_f32_16x16x32_f16 v[20:23], v[52:55], v[76:79], v[20:23]
	v_mfma_f32_16x16x32_f16 v[16:19], v[60:63], v[76:79], v[16:19]
	v_mfma_f32_16x16x32_f16 v[12:15], v[52:55], v[84:87], v[12:15]
	v_mfma_f32_16x16x32_f16 v[8:11], v[60:63], v[84:87], v[8:11]
	v_mfma_f32_16x16x32_f16 v[4:7], v[52:55], v[92:95], v[4:7]
	v_mfma_f32_16x16x32_f16 v[0:3], v[60:63], v[92:95], v[0:3]
	s_setprio 0
	s_barrier
	s_mov_b32 m0, s38
	v_lshl_add_u64 v[42:43], s[58:59], 0, v[34:35]
	global_load_lds_dwordx4 v[42:43], off
	v_lshl_add_u64 v[96:97], s[58:59], 0, v[38:39]
	s_mov_b32 m0, s39
	v_lshl_add_u64 v[98:99], s[56:57], 0, v[32:33]
	global_load_lds_dwordx4 v[96:97], off
	s_mov_b32 m0, s37
	s_nop 0
	global_load_lds_dwordx4 v[98:99], off
	v_lshl_add_u64 v[100:101], s[56:57], 0, v[36:37]
	s_mov_b32 m0, s40
	s_nop 0
	global_load_lds_dwordx4 v[100:101], off
	s_waitcnt vmcnt(4)
	s_barrier
	s_barrier
	ds_read_b128 v[48:51], v46 offset:49152
	ds_read_b128 v[52:55], v46 offset:50176
	ds_read_b128 v[56:59], v46 offset:51200
	ds_read_b128 v[60:63], v46 offset:52224
	ds_read_b128 v[64:67], v47 offset:16384
	ds_read_b128 v[68:71], v47 offset:17408
	ds_read_b128 v[72:75], v47 offset:18432
	ds_read_b128 v[76:79], v47 offset:19456
	ds_read_b128 v[80:83], v47 offset:20480
	ds_read_b128 v[84:87], v47 offset:21504
	ds_read_b128 v[88:91], v47 offset:22528
	ds_read_b128 v[92:95], v47 offset:23552
	s_waitcnt lgkmcnt(0)
	s_barrier
	s_waitcnt lgkmcnt(0)
	s_setprio 1
	s_waitcnt lgkmcnt(0)
	v_mfma_f32_16x16x32_f16 v[28:31], v[48:51], v[64:67], v[28:31]
	v_mfma_f32_16x16x32_f16 v[24:27], v[56:59], v[64:67], v[24:27]
	v_mfma_f32_16x16x32_f16 v[20:23], v[48:51], v[72:75], v[20:23]
	v_mfma_f32_16x16x32_f16 v[16:19], v[56:59], v[72:75], v[16:19]
	v_mfma_f32_16x16x32_f16 v[12:15], v[48:51], v[80:83], v[12:15]
	v_mfma_f32_16x16x32_f16 v[8:11], v[56:59], v[80:83], v[8:11]
	v_mfma_f32_16x16x32_f16 v[4:7], v[48:51], v[88:91], v[4:7]
	v_mfma_f32_16x16x32_f16 v[0:3], v[56:59], v[88:91], v[0:3]
	v_mfma_f32_16x16x32_f16 v[28:31], v[52:55], v[68:71], v[28:31]
	v_mfma_f32_16x16x32_f16 v[24:27], v[60:63], v[68:71], v[24:27]
	v_mfma_f32_16x16x32_f16 v[20:23], v[52:55], v[76:79], v[20:23]
	v_mfma_f32_16x16x32_f16 v[16:19], v[60:63], v[76:79], v[16:19]
	v_mfma_f32_16x16x32_f16 v[12:15], v[52:55], v[84:87], v[12:15]
	v_mfma_f32_16x16x32_f16 v[8:11], v[60:63], v[84:87], v[8:11]
	v_mfma_f32_16x16x32_f16 v[4:7], v[52:55], v[92:95], v[4:7]
	v_mfma_f32_16x16x32_f16 v[0:3], v[60:63], v[92:95], v[0:3]
	s_setprio 0
	s_barrier
	s_mov_b32 m0, s43
	v_lshl_add_u64 v[42:43], v[42:43], 0, s[18:19]
	global_load_lds_dwordx4 v[42:43], off
	v_lshl_add_u64 v[42:43], v[96:97], 0, s[18:19]
	s_mov_b32 m0, s44
	s_nop 0
	global_load_lds_dwordx4 v[42:43], off
	v_lshl_add_u64 v[42:43], v[98:99], 0, s[18:19]
	s_mov_b32 m0, s45
	s_nop 0
	global_load_lds_dwordx4 v[42:43], off
	v_lshl_add_u64 v[42:43], v[100:101], 0, s[18:19]
	s_mov_b32 m0, s46
	s_nop 0
	global_load_lds_dwordx4 v[42:43], off
	s_add_u32 s24, s24, 0x100
	s_addc_u32 s25, s25, 0
	s_waitcnt vmcnt(4)
	s_add_u32 s22, s22, 0x100
	s_addc_u32 s23, s23, 0
	s_cmp_ge_i32 s60, s48
	s_mov_b32 s55, s60
	s_barrier
	s_barrier
	s_cbranch_scc0 .LBB1_21
	s_branch .LBB1_8
